# v72 + attention: the four partial-output read-backs of each sub-tile (selected and window branches) issued together behind one wait
# baseline (speedup 1.0000x reference)
; __device__ __forceinline__ unsigned cvt_pk_bf16(float lo, float hi) { const f32x2_t v = {lo, hi}; const bf16x2_t b = __builtin_convertvector(v, bf16x2_t); return __builtin_bit_cast(unsigned, b); }
; #define GATE(rb, br) (GATES[TOKROW(rb) * 48 + head * 3 + (br)])
; __device__ __forceinline__ void ph_attn_fast2(const Args& a, LAS unsigned char* lds) {
;     ...
;                 for (int rb = 0; rb < 2; ++rb) { const float l = __shfl(ss[rb].ol[0], fr); const float sc1 = (l > 0.f) ? GATE(rb, 1) / l : 0.f;
;                     bf16_t* op = O + TOKROW(rb) * 1024 + head * 64 + 4 * g4;
; #pragma unroll
;                     for (int dt = 0; dt < 4; ++dt) { const u32x2 pv = *(const u32x2*)(op + 16 * dt); f32x4 v = ss[rb].o[dt] * sc1;
;                         v[0] += __uint_as_float(pv.x << 16); v[1] += __uint_as_float(pv.x & 0xffff0000u); v[2] += __uint_as_float(pv.y << 16); v[3] += __uint_as_float(pv.y & 0xffff0000u);
;                         u32x2 w; w.x = cvt_pk_bf16(v[0], v[1]); w.y = cvt_pk_bf16(v[2], v[3]); *(u32x2*)(op + 16 * dt) = w; } }
;     ...
;                 AT_DMA(2, jt0, 0); if (nt_ > 1) AT_DMA(2, jt0 + 1, 1); __syncthreads();
.LBB0_2119:
	s_or_b64 exec, exec, s[2:3]
	v_lshlrev_b64 v[36:37], 11, v[108:109]
	v_lshl_add_u64 v[36:37], v[178:179], 0, v[36:37]
	global_load_dwordx2 v[62:63], v[36:37], off
	global_load_dwordx2 v[66:67], v[36:37], off offset:32
	global_load_dwordx2 v[68:69], v[36:37], off offset:64
	global_load_dwordx2 v[70:71], v[36:37], off offset:96
	ds_bpermute_b32 v1, v243, v34
	v_ashrrev_i32_e32 v107, 31, v106
	s_waitcnt lgkmcnt(0)
	v_cmp_lt_f32_e32 vcc, 0, v1
	s_waitcnt vmcnt(0)
	v_lshlrev_b32_e32 v64, 16, v62
	v_and_b32_e32 v65, 0xffff0000, v62
	v_lshlrev_b32_e32 v62, 16, v63
	v_and_b32_e32 v63, 0xffff0000, v63
	v_pk_fma_f32 v[46:47], v[46:47], v[4:5], v[64:65] op_sel_hi:[1,0,1]
	v_pk_fma_f32 v[48:49], v[48:49], v[4:5], v[62:63] op_sel_hi:[1,0,1]
	v_cvt_pk_bf16_f32 v46, v46, v47
	v_cvt_pk_bf16_f32 v47, v48, v49
	global_store_dwordx2 v[36:37], v[46:47], off
	v_lshlrev_b32_e32 v48, 16, v66
	v_and_b32_e32 v49, 0xffff0000, v66
	v_lshlrev_b32_e32 v46, 16, v67
	v_and_b32_e32 v47, 0xffff0000, v67
	v_pk_fma_f32 v[48:49], v[50:51], v[4:5], v[48:49] op_sel_hi:[1,0,1]
	v_pk_fma_f32 v[46:47], v[52:53], v[4:5], v[46:47] op_sel_hi:[1,0,1]
	v_cvt_pk_bf16_f32 v48, v48, v49
	v_cvt_pk_bf16_f32 v49, v46, v47
	global_store_dwordx2 v[36:37], v[48:49], off offset:32
	v_lshlrev_b32_e32 v48, 16, v68
	v_and_b32_e32 v49, 0xffff0000, v68
	v_lshlrev_b32_e32 v46, 16, v69
	v_and_b32_e32 v47, 0xffff0000, v69
	v_pk_fma_f32 v[48:49], v[54:55], v[4:5], v[48:49] op_sel_hi:[1,0,1]
	v_pk_fma_f32 v[46:47], v[56:57], v[4:5], v[46:47] op_sel_hi:[1,0,1]
	v_cvt_pk_bf16_f32 v48, v48, v49
	v_cvt_pk_bf16_f32 v49, v46, v47
	global_store_dwordx2 v[36:37], v[48:49], off offset:64
	v_lshlrev_b32_e32 v48, 16, v70
	v_and_b32_e32 v49, 0xffff0000, v70
	v_lshlrev_b32_e32 v46, 16, v71
	v_and_b32_e32 v47, 0xffff0000, v71
	v_pk_fma_f32 v[48:49], v[58:59], v[4:5], v[48:49] op_sel_hi:[1,0,1]
	v_pk_fma_f32 v[4:5], v[60:61], v[4:5], v[46:47] op_sel_hi:[1,0,1]
	v_cvt_pk_bf16_f32 v46, v48, v49
	v_cvt_pk_bf16_f32 v47, v4, v5
	global_store_dwordx2 v[36:37], v[46:47], off offset:96
	s_and_saveexec_b64 s[2:3], vcc
	s_cbranch_execz .LBB0_2121
	v_readlane_b32 s6, v252, 59
	v_readlane_b32 s7, v252, 60
	s_movk_i32 s5, 0xc0
	s_nop 0
	v_lshl_add_u64 v[4:5], s[6:7], 0, v[106:107]
	v_mad_u64_u32 v[34:35], s[6:7], v4, s5, v[174:175]
	v_mad_i32_i24 v35, v5, s5, v35
	global_load_dword v2, v[34:35], off offset:4
	s_waitcnt vmcnt(0)
	v_div_scale_f32 v4, s[6:7], v1, v1, v2
	v_rcp_f32_e32 v5, v4
	v_div_scale_f32 v34, vcc, v2, v1, v2
	v_fma_f32 v35, -v4, v5, 1.0
	v_fmac_f32_e32 v5, v35, v5
	v_mul_f32_e32 v35, v34, v5
	v_fma_f32 v36, -v4, v35, v34
	v_fmac_f32_e32 v35, v36, v5
	v_fma_f32 v4, -v4, v35, v34
	v_div_fmas_f32 v4, v4, v5, v35
	v_div_fixup_f32 v2, v4, v1, v2
.LBB0_2121:
	s_or_b64 exec, exec, s[2:3]
	v_lshlrev_b64 v[4:5], 11, v[106:107]
	v_lshl_add_u64 v[4:5], v[178:179], 0, v[4:5]
	global_load_dwordx2 v[34:35], v[4:5], off
	global_load_dwordx2 v[72:73], v[4:5], off offset:32
	global_load_dwordx2 v[74:75], v[4:5], off offset:64
	global_load_dwordx2 v[76:77], v[4:5], off offset:96
	s_ashr_i32 s5, s4, 31
	s_sub_i32 s22, s83, s4
	s_lshl_b64 s[6:7], s[4:5], 13
	s_add_u32 s2, s8, s6
	v_readlane_b32 s5, v252, 39
	s_addc_u32 s3, s9, s7
	s_mov_b32 m0, s5
	v_mov_b32_e32 v159, v3
	global_load_lds_dwordx4 v156, s[2:3]
	s_mov_b32 s5, s9
	s_cmp_lt_i32 s22, 1
	s_waitcnt vmcnt(0)
	v_lshlrev_b32_e32 v36, 16, v34
	v_and_b32_e32 v37, 0xffff0000, v34
	v_lshlrev_b32_e32 v34, 16, v35
	v_and_b32_e32 v35, 0xffff0000, v35
	v_pk_fma_f32 v[36:37], v[42:43], v[2:3], v[36:37] op_sel_hi:[1,0,1]
	v_pk_fma_f32 v[34:35], v[44:45], v[2:3], v[34:35] op_sel_hi:[1,0,1]
	v_cvt_pk_bf16_f32 v36, v36, v37
	v_cvt_pk_bf16_f32 v37, v34, v35
	global_store_dwordx2 v[4:5], v[36:37], off
	v_lshlrev_b32_e32 v36, 16, v72
	v_and_b32_e32 v37, 0xffff0000, v72
	v_lshlrev_b32_e32 v34, 16, v73
	v_and_b32_e32 v35, 0xffff0000, v73
	v_pk_fma_f32 v[36:37], v[38:39], v[2:3], v[36:37] op_sel_hi:[1,0,1]
	v_pk_fma_f32 v[34:35], v[40:41], v[2:3], v[34:35] op_sel_hi:[1,0,1]
	v_cvt_pk_bf16_f32 v36, v36, v37
	v_cvt_pk_bf16_f32 v37, v34, v35
	global_store_dwordx2 v[4:5], v[36:37], off offset:32
	v_lshlrev_b32_e32 v36, 16, v74
	v_and_b32_e32 v37, 0xffff0000, v74
	v_lshlrev_b32_e32 v34, 16, v75
	v_and_b32_e32 v35, 0xffff0000, v75
	v_pk_fma_f32 v[30:31], v[30:31], v[2:3], v[36:37] op_sel_hi:[1,0,1]
	v_pk_fma_f32 v[32:33], v[32:33], v[2:3], v[34:35] op_sel_hi:[1,0,1]
	v_cvt_pk_bf16_f32 v30, v30, v31
	v_cvt_pk_bf16_f32 v31, v32, v33
	global_store_dwordx2 v[4:5], v[30:31], off offset:64
	v_lshlrev_b32_e32 v32, 16, v76
	v_and_b32_e32 v33, 0xffff0000, v76
	v_lshlrev_b32_e32 v30, 16, v77
	v_and_b32_e32 v31, 0xffff0000, v77
	v_pk_fma_f32 v[26:27], v[26:27], v[2:3], v[32:33] op_sel_hi:[1,0,1]
	v_pk_fma_f32 v[28:29], v[28:29], v[2:3], v[30:31] op_sel_hi:[1,0,1]
	v_cvt_pk_bf16_f32 v26, v26, v27
	v_cvt_pk_bf16_f32 v27, v28, v29
	global_store_dwordx2 v[4:5], v[26:27], off offset:96
	v_lshl_add_u64 v[4:5], s[2:3], 0, v[158:159]
	s_mov_b32 s3, s8
	s_mov_b64 s[8:9], 0x1000000
	v_readlane_b32 s2, v252, 34
	v_lshl_add_u64 v[4:5], v[4:5], 0, s[8:9]
	s_mov_b32 m0, s2
	s_nop 0
	global_load_lds_dwordx4 v[4:5], off
	s_cbranch_scc1 .LBB0_2123
	v_readlane_b32 s2, v252, 35
	s_mov_b32 m0, s2
	s_add_u32 s2, s3, s6
	s_addc_u32 s3, s5, s7
	s_add_u32 s2, s2, 0x2000
	s_addc_u32 s3, s3, 0
	v_lshl_add_u64 v[4:5], s[2:3], 0, v[158:159]
	global_load_lds_dwordx4 v156, s[2:3]
	v_readlane_b32 s2, v252, 36
	v_lshl_add_u64 v[4:5], v[4:5], 0, s[8:9]
	s_mov_b32 m0, s2
	s_nop 0
	global_load_lds_dwordx4 v[4:5], off

; __device__ __forceinline__ unsigned pk4_fp8(float a, float b, float c, float d) { int w = __builtin_amdgcn_cvt_pk_fp8_f32(a, b, 0, false); return (unsigned)__builtin_amdgcn_cvt_pk_fp8_f32(c, d, w, true); }
; __device__ __forceinline__ float clamp8(float v) { return __builtin_amdgcn_fmed3f(v, -448.0f, 448.0f); }
; #define GATE(rb, br) (GATES[TOKROW(rb) * 48 + head * 3 + (br)])
; __device__ __forceinline__ void ph_attn_fast2(const Args& a, LAS unsigned char* lds) {
;     ...
;                 for (int rb = 0; rb < 2; ++rb) { const float l = __shfl(sw[rb].ol[0], fr); const float sc2 = (l > 0.f) ? GATE(rb, 2) / l : 0.f;
;                     bf16_t* op = O + TOKROW(rb) * 1024 + head * 64 + 4 * g4;
;                     unsigned char* o8 = (unsigned char*)(a.ws + WS_O8) + TOKROW(rb) * 1024 + head * 64 + 4 * g4;
; #pragma unroll
;                     for (int dt = 0; dt < 4; ++dt) { const u32x2 pv = *(const u32x2*)(op + 16 * dt); f32x4 v = sw[rb].o[dt] * sc2;
;                         v[0] += __uint_as_float(pv.x << 16); v[1] += __uint_as_float(pv.x & 0xffff0000u); v[2] += __uint_as_float(pv.y << 16); v[3] += __uint_as_float(pv.y & 0xffff0000u);
;                         *(unsigned*)(o8 + 16 * dt) = pk4_fp8(clamp8(v[0] * X8_SCALE), clamp8(v[1] * X8_SCALE), clamp8(v[2] * X8_SCALE), clamp8(v[3] * X8_SCALE)); } }
.LBB0_2178:
	s_or_b64 exec, exec, s[0:1]
	v_readlane_b32 s6, v252, 63
	v_lshlrev_b64 v[4:5], 10, v[108:109]
	v_readlane_b32 s7, v251, 0
	v_pk_mul_f32 v[16:17], v[60:61], v[10:11] op_sel_hi:[1,0]
	v_pk_mul_f32 v[18:19], v[58:59], v[10:11] op_sel_hi:[1,0]
	v_lshl_add_u64 v[4:5], v[4:5], 0, s[6:7]
	v_lshl_add_u64 v[12:13], v[4:5], 1, v[172:173]
	global_load_dwordx2 v[14:15], v[12:13], off
	global_load_dwordx2 v[66:67], v[12:13], off offset:32
	global_load_dwordx2 v[68:69], v[12:13], off offset:64
	global_load_dwordx2 v[70:71], v[12:13], off offset:96
	s_mov_b32 s5, 0xc3e00000
	v_lshl_add_u64 v[4:5], v[204:205], 0, v[4:5]
	v_ashrrev_i32_e32 v107, 31, v106
	s_waitcnt vmcnt(0)
	v_lshlrev_b32_e32 v1, 16, v14
	v_and_b32_e32 v11, 0xffff0000, v14
	v_add_f32_e32 v1, v18, v1
	v_add_f32_e32 v11, v19, v11
	v_lshlrev_b32_e32 v14, 16, v15
	v_mul_f32_e32 v1, 0x41000000, v1
	v_mul_f32_e32 v11, 0x41000000, v11
	v_add_f32_e32 v14, v16, v14
	v_med3_f32 v1, v1, s5, v249
	v_med3_f32 v11, v11, s5, v249
	v_mov_b32_e32 v16, v3
	v_and_b32_e32 v15, 0xffff0000, v15
	v_cvt_pk_fp8_f32 v16, v1, v11
	v_add_f32_e32 v15, v17, v15
	v_mul_f32_e32 v14, 0x41000000, v14
	v_mul_f32_e32 v15, 0x41000000, v15
	v_med3_f32 v14, v14, s5, v249
	v_med3_f32 v15, v15, s5, v249
	v_cvt_pk_fp8_f32 v16, v14, v15 op_sel:[0,0,1]
	v_pk_mul_f32 v[18:19], v[54:55], v[10:11] op_sel_hi:[1,0]
	global_store_dword v[4:5], v16, off
	v_pk_mul_f32 v[16:17], v[56:57], v[10:11] op_sel_hi:[1,0]
	v_lshlrev_b32_e32 v1, 16, v66
	v_and_b32_e32 v11, 0xffff0000, v66
	v_add_f32_e32 v1, v18, v1
	v_add_f32_e32 v11, v19, v11
	v_lshlrev_b32_e32 v14, 16, v67
	v_mul_f32_e32 v1, 0x41000000, v1
	v_mul_f32_e32 v11, 0x41000000, v11
	v_add_f32_e32 v14, v16, v14
	v_med3_f32 v1, v1, s5, v249
	v_med3_f32 v11, v11, s5, v249
	v_mov_b32_e32 v16, v3
	v_and_b32_e32 v15, 0xffff0000, v67
	v_cvt_pk_fp8_f32 v16, v1, v11
	v_add_f32_e32 v15, v17, v15
	v_mul_f32_e32 v14, 0x41000000, v14
	v_mul_f32_e32 v15, 0x41000000, v15
	v_med3_f32 v14, v14, s5, v249
	v_med3_f32 v15, v15, s5, v249
	v_cvt_pk_fp8_f32 v16, v14, v15 op_sel:[0,0,1]
	v_pk_mul_f32 v[18:19], v[46:47], v[10:11] op_sel_hi:[1,0]
	global_store_dword v[4:5], v16, off offset:16
	v_pk_mul_f32 v[16:17], v[48:49], v[10:11] op_sel_hi:[1,0]
	v_lshlrev_b32_e32 v1, 16, v68
	v_and_b32_e32 v11, 0xffff0000, v68
	v_add_f32_e32 v1, v18, v1
	v_add_f32_e32 v11, v19, v11
	v_lshlrev_b32_e32 v14, 16, v69
	v_mul_f32_e32 v1, 0x41000000, v1
	v_mul_f32_e32 v11, 0x41000000, v11
	v_add_f32_e32 v14, v16, v14
	v_med3_f32 v1, v1, s5, v249
	v_med3_f32 v11, v11, s5, v249
	v_mov_b32_e32 v16, v3
	v_and_b32_e32 v15, 0xffff0000, v69
	v_cvt_pk_fp8_f32 v16, v1, v11
	v_add_f32_e32 v15, v17, v15
	v_mul_f32_e32 v14, 0x41000000, v14
	v_mul_f32_e32 v15, 0x41000000, v15
	v_med3_f32 v14, v14, s5, v249
	v_med3_f32 v15, v15, s5, v249
	v_cvt_pk_fp8_f32 v16, v14, v15 op_sel:[0,0,1]
	v_pk_mul_f32 v[14:15], v[52:53], v[10:11] op_sel_hi:[1,0]
	v_pk_mul_f32 v[10:11], v[50:51], v[10:11] op_sel_hi:[1,0]
	global_store_dword v[4:5], v16, off offset:32
	v_lshlrev_b32_e32 v1, 16, v70
	v_add_f32_e32 v1, v10, v1
	v_and_b32_e32 v10, 0xffff0000, v70
	v_add_f32_e32 v10, v11, v10
	v_mul_f32_e32 v1, 0x41000000, v1
	v_mul_f32_e32 v10, 0x41000000, v10
	v_lshlrev_b32_e32 v11, 16, v71
	v_and_b32_e32 v12, 0xffff0000, v71
	v_med3_f32 v1, v1, s5, v249
	v_med3_f32 v10, v10, s5, v249
	v_mov_b32_e32 v13, v3
	v_cvt_pk_fp8_f32 v13, v1, v10
	v_add_f32_e32 v11, v14, v11
	v_add_f32_e32 v12, v15, v12
	v_mul_f32_e32 v11, 0x41000000, v11
	v_mul_f32_e32 v12, 0x41000000, v12
	ds_bpermute_b32 v1, v243, v38
	v_med3_f32 v11, v11, s5, v249
	v_med3_f32 v12, v12, s5, v249
	v_cvt_pk_fp8_f32 v13, v11, v12 op_sel:[0,0,1]
	s_waitcnt lgkmcnt(0)
	v_cmp_lt_f32_e32 vcc, 0, v1
	global_store_dword v[4:5], v13, off offset:48
	s_and_saveexec_b64 s[0:1], vcc
	v_readlane_b32 s58, v252, 7
	v_readlane_b32 s60, v252, 42
	v_readlane_b32 s62, v252, 44
	v_readlane_b32 s64, v252, 54
	v_readlane_b32 s59, v252, 8
	v_readlane_b32 s57, v252, 58
	v_readlane_b32 s61, v252, 43
	v_readlane_b32 s63, v252, 45
	v_readlane_b32 s65, v252, 55
	v_readlane_b32 s66, v252, 52
	v_readlane_b32 s67, v252, 53
	v_readlane_b32 s68, v252, 32
	v_readlane_b32 s69, v252, 33
	v_readlane_b32 s70, v251, 3
	s_cbranch_execz .LBB0_2180
	v_readlane_b32 s2, v252, 59
	v_readlane_b32 s3, v252, 60
	s_movk_i32 s4, 0xc0
	s_nop 0
	v_lshl_add_u64 v[4:5], s[2:3], 0, v[106:107]
	v_mad_u64_u32 v[10:11], s[2:3], v4, s4, v[174:175]
	v_mad_i32_i24 v11, v5, s4, v11
	global_load_dword v2, v[10:11], off offset:8
	s_waitcnt vmcnt(0)
	v_div_scale_f32 v4, s[2:3], v1, v1, v2
	v_rcp_f32_e32 v5, v4
	v_div_scale_f32 v10, vcc, v2, v1, v2
	v_fma_f32 v11, -v4, v5, 1.0
	v_fmac_f32_e32 v5, v11, v5
	v_mul_f32_e32 v11, v10, v5
	v_fma_f32 v12, -v4, v11, v10
	v_fmac_f32_e32 v11, v12, v5
	v_fma_f32 v4, -v4, v11, v10
	v_div_fmas_f32 v4, v4, v5, v11
	v_div_fixup_f32 v2, v4, v1, v2
; #define LAS __attribute__((address_space(3)))
; __device__ __forceinline__ unsigned pk4_fp8(float a, float b, float c, float d) { int w = __builtin_amdgcn_cvt_pk_fp8_f32(a, b, 0, false); return (unsigned)__builtin_amdgcn_cvt_pk_fp8_f32(c, d, w, true); }
; __device__ __forceinline__ float clamp8(float v) { return __builtin_amdgcn_fmed3f(v, -448.0f, 448.0f); }
; __device__ __forceinline__ void ph_attn_fast2(const Args& a, LAS unsigned char* lds) {
;     ...
;                 for (int rb = 0; rb < 2; ++rb) { const float l = __shfl(sw[rb].ol[0], fr); const float sc2 = (l > 0.f) ? GATE(rb, 2) / l : 0.f;
;                     bf16_t* op = O + TOKROW(rb) * 1024 + head * 64 + 4 * g4;
;                     unsigned char* o8 = (unsigned char*)(a.ws + WS_O8) + TOKROW(rb) * 1024 + head * 64 + 4 * g4;
; #pragma unroll
;                     for (int dt = 0; dt < 4; ++dt) { const u32x2 pv = *(const u32x2*)(op + 16 * dt); f32x4 v = sw[rb].o[dt] * sc2;
;                         v[0] += __uint_as_float(pv.x << 16); v[1] += __uint_as_float(pv.x & 0xffff0000u); v[2] += __uint_as_float(pv.y << 16); v[3] += __uint_as_float(pv.y & 0xffff0000u);
;                         *(unsigned*)(o8 + 16 * dt) = pk4_fp8(clamp8(v[0] * X8_SCALE), clamp8(v[1] * X8_SCALE), clamp8(v[2] * X8_SCALE), clamp8(v[3] * X8_SCALE)); } }
;     ...
;             {
;                 const int npr = half ? pr + (int)gridDim.x : pr, nhalf = half ^ 1;
;                 cmp_pref = npr < 1024;
;                 if (cmp_pref) { const int nbg = npr >> 6, npp = attn_pair_of(npr), ncc = nhalf ? (127 - npp) : npp;
;                     const int nnct = (((ncc * 64 + 63 - 31) / 16 + 1) + 63) >> 6;
;                     const bf16_t* nk = KC + (size_t)nbg * 512 * 64;
;                     __builtin_amdgcn_global_load_lds((const unsigned*)(nk + ksrc), (LAS unsigned*)(lds + AT4_KB + wave * 1024), 16, 0, 0);
;                     __builtin_amdgcn_global_load_lds((const unsigned*)(nk + (size_t)8192 * 64 + vsrc), (LAS unsigned*)(lds + AT4_VB + wave * 1024), 16, 0, 0);
;                     if (nnct > 1) {
;                         __builtin_amdgcn_global_load_lds((const unsigned*)(nk + 4096 + ksrc), (LAS unsigned*)(lds + AT4_KB + 8192 + wave * 1024), 16, 0, 0);
;                         __builtin_amdgcn_global_load_lds((const unsigned*)(nk + (size_t)8192 * 64 + 4096 + vsrc), (LAS unsigned*)(lds + AT4_VB + 8192 + wave * 1024), 16, 0, 0); } } }
.LBB0_2180:
	s_or_b64 exec, exec, s[0:1]
	v_lshlrev_b64 v[4:5], 10, v[106:107]
	v_lshl_add_u64 v[4:5], v[4:5], 0, s[6:7]
	v_lshl_add_u64 v[10:11], v[4:5], 1, v[172:173]
	global_load_dwordx2 v[12:13], v[10:11], off
	global_load_dwordx2 v[72:73], v[10:11], off offset:32
	global_load_dwordx2 v[74:75], v[10:11], off offset:64
	global_load_dwordx2 v[76:77], v[10:11], off offset:96
	v_pk_mul_f32 v[16:17], v[42:43], v[2:3] op_sel_hi:[1,0]
	v_pk_mul_f32 v[14:15], v[44:45], v[2:3] op_sel_hi:[1,0]
	v_lshl_add_u64 v[4:5], v[204:205], 0, v[4:5]
	v_readlane_b32 s0, v251, 9
	v_readlane_b32 s1, v251, 10
	s_and_b64 s[0:1], s[0:1], exec
	v_readlane_b32 s0, v252, 11
	s_cselect_b32 s2, 0, s0
	s_add_i32 s2, s2, s57
	s_cmpk_lt_i32 s2, 0x400
	s_cselect_b64 s[0:1], -1, 0
	s_cmpk_gt_i32 s2, 0x3ff
	s_waitcnt vmcnt(0)
	v_lshlrev_b32_e32 v1, 16, v12
	v_and_b32_e32 v12, 0xffff0000, v12
	v_add_f32_e32 v1, v16, v1
	v_add_f32_e32 v12, v17, v12
	v_lshlrev_b32_e32 v16, 16, v13
	v_and_b32_e32 v13, 0xffff0000, v13
	v_mul_f32_e32 v1, 0x41000000, v1
	v_mul_f32_e32 v12, 0x41000000, v12
	v_add_f32_e32 v13, v15, v13
	v_med3_f32 v1, v1, s5, v249
	v_med3_f32 v12, v12, s5, v249
	v_mov_b32_e32 v15, v3
	v_cvt_pk_fp8_f32 v15, v1, v12
	v_add_f32_e32 v14, v14, v16
	v_mul_f32_e32 v14, 0x41000000, v14
	v_mul_f32_e32 v13, 0x41000000, v13
	v_med3_f32 v14, v14, s5, v249
	v_med3_f32 v13, v13, s5, v249
	v_cvt_pk_fp8_f32 v15, v14, v13 op_sel:[0,0,1]
	v_pk_mul_f32 v[16:17], v[34:35], v[2:3] op_sel_hi:[1,0]
	global_store_dword v[4:5], v15, off
	v_pk_mul_f32 v[14:15], v[36:37], v[2:3] op_sel_hi:[1,0]
	v_lshlrev_b32_e32 v1, 16, v72
	v_and_b32_e32 v12, 0xffff0000, v72
	v_add_f32_e32 v1, v16, v1
	v_add_f32_e32 v12, v17, v12
	v_lshlrev_b32_e32 v16, 16, v73
	v_and_b32_e32 v13, 0xffff0000, v73
	v_mul_f32_e32 v1, 0x41000000, v1
	v_mul_f32_e32 v12, 0x41000000, v12
	v_add_f32_e32 v13, v15, v13
	v_med3_f32 v1, v1, s5, v249
	v_med3_f32 v12, v12, s5, v249
	v_mov_b32_e32 v15, v3
	v_cvt_pk_fp8_f32 v15, v1, v12
	v_add_f32_e32 v14, v14, v16
	v_mul_f32_e32 v14, 0x41000000, v14
	v_mul_f32_e32 v13, 0x41000000, v13
	v_med3_f32 v14, v14, s5, v249
	v_med3_f32 v13, v13, s5, v249
	v_cvt_pk_fp8_f32 v15, v14, v13 op_sel:[0,0,1]
	v_pk_mul_f32 v[16:17], v[30:31], v[2:3] op_sel_hi:[1,0]
	global_store_dword v[4:5], v15, off offset:16
	v_pk_mul_f32 v[14:15], v[32:33], v[2:3] op_sel_hi:[1,0]
	v_lshlrev_b32_e32 v1, 16, v74
	v_and_b32_e32 v12, 0xffff0000, v74
	v_add_f32_e32 v1, v16, v1
	v_add_f32_e32 v12, v17, v12
	v_lshlrev_b32_e32 v16, 16, v75
	v_and_b32_e32 v13, 0xffff0000, v75
	v_mul_f32_e32 v1, 0x41000000, v1
	v_mul_f32_e32 v12, 0x41000000, v12
	v_add_f32_e32 v13, v15, v13
	v_med3_f32 v1, v1, s5, v249
	v_med3_f32 v12, v12, s5, v249
	v_mov_b32_e32 v15, v3
	v_cvt_pk_fp8_f32 v15, v1, v12
	v_add_f32_e32 v14, v14, v16
	v_mul_f32_e32 v14, 0x41000000, v14
	v_mul_f32_e32 v13, 0x41000000, v13
	v_med3_f32 v14, v14, s5, v249
	v_med3_f32 v13, v13, s5, v249
	v_cvt_pk_fp8_f32 v15, v14, v13 op_sel:[0,0,1]
	v_pk_mul_f32 v[12:13], v[28:29], v[2:3] op_sel_hi:[1,0]
	global_store_dword v[4:5], v15, off offset:32
	v_pk_mul_f32 v[14:15], v[26:27], v[2:3] op_sel_hi:[1,0]
	v_lshlrev_b32_e32 v1, 16, v76
	v_and_b32_e32 v2, 0xffff0000, v76
	v_add_f32_e32 v1, v14, v1
	v_add_f32_e32 v2, v15, v2
	v_lshlrev_b32_e32 v10, 16, v77
	v_mul_f32_e32 v1, 0x41000000, v1
	v_mul_f32_e32 v2, 0x41000000, v2
	v_add_f32_e32 v10, v12, v10
	v_med3_f32 v1, v1, s5, v249
	v_med3_f32 v2, v2, s5, v249
	v_mov_b32_e32 v12, v3
	v_and_b32_e32 v11, 0xffff0000, v77
	v_cvt_pk_fp8_f32 v12, v1, v2
	v_add_f32_e32 v11, v13, v11
	v_mul_f32_e32 v10, 0x41000000, v10
	v_mul_f32_e32 v11, 0x41000000, v11
	v_med3_f32 v10, v10, s5, v249
	v_med3_f32 v11, v11, s5, v249
	v_cvt_pk_fp8_f32 v12, v10, v11 op_sel:[0,0,1]
	global_store_dword v[4:5], v12, off offset:48
	s_cbranch_scc1 .LBB0_2183
	v_readlane_b32 s3, v252, 39
	s_lshr_b32 s5, s2, 4
	s_mov_b32 m0, s3
	s_and_b32 s3, s2, 63
	s_and_b32 s5, s5, 32
	s_xor_b32 s3, s5, s3
	s_lshl_b32 s3, s3, 2
	s_ashr_i32 s4, s2, 6
	s_and_b32 s2, s2, 0x100
	s_xor_b32 s5, s3, 0xfc
	s_cmp_eq_u32 s2, 0
	s_cselect_b32 s5, s3, s5
	v_readlane_b32 s2, v251, 6
	s_xor_b32 s6, s5, 0x1fc
	v_readlane_b32 s3, v251, 7
	s_and_b64 s[2:3], s[2:3], exec
	s_cselect_b32 s6, s5, s6
	s_ashr_i32 s5, s4, 31
	s_lshl_b64 s[2:3], s[4:5], 16
	v_readlane_b32 s4, v252, 23
	s_add_u32 s2, s4, s2
	v_readlane_b32 s4, v252, 24
	s_addc_u32 s3, s4, s3
	v_mov_b32_e32 v159, v3
	v_lshl_add_u64 v[4:5], s[2:3], 0, v[158:159]
	s_mov_b64 s[4:5], 0x100000
	v_lshl_add_u64 v[10:11], v[4:5], 0, s[4:5]
	v_readlane_b32 s4, v252, 34
	global_load_lds_dwordx4 v156, s[2:3]
	s_mov_b32 m0, s4
	s_cmp_lt_u32 s6, 62
	global_load_lds_dwordx4 v[10:11], off
	s_cbranch_scc1 .LBB0_2183
	v_mov_b32_e32 v157, v3
	v_lshl_add_u64 v[10:11], s[2:3], 0, v[156:157]
	s_mov_b64 s[2:3], 0x2000
	v_readlane_b32 s4, v252, 35
	v_lshl_add_u64 v[10:11], v[10:11], 0, s[2:3]
	s_mov_b64 s[2:3], 0x102000
	s_mov_b32 m0, s4
	v_lshl_add_u64 v[4:5], v[4:5], 0, s[2:3]
	v_readlane_b32 s2, v252, 36
	global_load_lds_dwordx4 v[10:11], off
	s_mov_b32 m0, s2
	s_nop 0
	global_load_lds_dwordx4 v[4:5], off
